# prologue: 4 static conversion rounds (8192 items) and only 512 items through the atomic work counter (was 2560), fold per SIMD in rounds 0/1, counter bypassed when nothing is left
# baseline (speedup 1.0000x reference)
.LBB0_41:
	v_writelane_b32 v253, s24, 32
	v_writelane_b32 v253, s23, 34
	v_writelane_b32 v253, s22, 36
	s_mov_b32 s3, 0
	v_readlane_b32 s0, v253, 29
	s_lshl_b32 s0, s0, 14
	s_add_i32 s29, s0, 0
	s_cmp_lg_u64 s[48:49], 0
	v_readlane_b32 s4, v253, 30
	s_cselect_b64 s[44:45], -1, 0
	s_abs_i32 s2, s4
	v_cvt_f32_u32_e32 v2, s2
	s_sub_i32 s0, 0, s2
	s_ashr_i32 s6, s4, 31
	v_rcp_iflag_f32_e32 v2, v2
	s_nop 0
	v_mul_f32_e32 v2, 0x4f7ffffe, v2
	v_cvt_u32_f32_e32 v2, v2
	s_nop 0
	v_readfirstlane_b32 s1, v2
	s_mul_i32 s0, s0, s1
	s_mul_hi_u32 s0, s1, s0
	s_add_i32 s7, s1, s0
	s_mul_hi_u32 s0, s7, 0x4200
	s_mul_i32 s0, s0, s2
	s_sub_i32 s0, 0x4200, s0
	s_sub_i32 s1, s0, s2
	s_cmp_ge_u32 s0, s2
	s_cselect_b32 s0, s1, s0
	s_sub_i32 s1, s0, s2
	s_cmp_ge_u32 s0, s2
	s_cselect_b32 s8, s1, s0
	s_add_i32 s0, s4, 0xffffff00
	s_cmp_ge_i32 s0, s8
	s_cselect_b64 s[0:1], -1, 0
	s_cmpk_lt_u32 s8, 0x2101
	s_cselect_b64 s[4:5], -1, 0
	s_sub_i32 s8, 0x4200, s8
	s_and_b64 s[0:1], s[0:1], s[4:5]
	s_and_b64 s[0:1], s[0:1], exec
	s_cselect_b32 s5, s8, 0x4200
	s_add_i32 s0, s5, 0xffffe200
	s_cmp_eq_u32 s2, 0x800
	s_cselect_b32 s5, s0, s5
	v_writelane_b32 v253, s5, 38
	v_writelane_b32 v253, s48, 40
	s_mul_hi_u32 s0, s5, s7
	s_mul_i32 s1, s0, s2
	v_writelane_b32 v253, s49, 41
	v_writelane_b32 v253, s50, 42
	v_writelane_b32 v253, s51, 43
	v_writelane_b32 v253, s52, 44
	v_writelane_b32 v253, s53, 45
	v_writelane_b32 v253, s54, 46
	v_writelane_b32 v253, s55, 47
	s_sub_i32 s1, s5, s1
	v_writelane_b32 v253, s56, 48
	s_add_i32 s4, s0, 1
	s_sub_i32 s5, s1, s2
	v_writelane_b32 v253, s57, 49
	s_cmp_ge_u32 s1, s2
	v_writelane_b32 v253, s58, 50
	s_cselect_b32 s0, s4, s0
	v_writelane_b32 v253, s59, 51
	s_cselect_b32 s1, s5, s1
	s_add_i32 s4, s0, 1
	v_writelane_b32 v253, s60, 52
	s_cmp_ge_u32 s1, s2
	v_writelane_b32 v253, s61, 53
	s_cselect_b32 s0, s4, s0
	v_writelane_b32 v253, s62, 54
	s_xor_b32 s0, s0, s6
	v_writelane_b32 v253, s63, 55
	s_sub_i32 s15, s0, s6
	v_writelane_b32 v253, s29, 56
	s_add_i32 s14, s15, 0
	v_writelane_b32 v253, s44, 57
	s_cmp_lt_i32 s15, 1
	v_readfirstlane_b32 s0, v0
	v_writelane_b32 v253, s45, 58
	s_cbranch_scc1 .LBB0_65
	s_ashr_i32 s0, s0, 8
	s_min_i32 s18, s0, s14
	s_cmpk_gt_i32 s27, 0x7ff
	v_readlane_b32 s0, v253, 26
	s_cselect_b64 s[20:21], -1, 0
	s_add_u32 s0, s0, 0x800000
	v_writelane_b32 v253, s0, 59
	v_mov_b32_e32 v133, 0
	v_readlane_b32 s0, v253, 27
	s_addc_u32 s0, s0, 0
	s_add_i32 s25, 0, 0x21000
	v_writelane_b32 v253, s0, 61
	s_add_i32 s0, 0, 0x21200
	v_writelane_b32 v253, s0, 63
	s_add_i32 s0, 0, 0x21100
	v_writelane_b32 v254, s0, 1
	s_add_i32 s0, 0, 0x21300
	v_writelane_b32 v254, s0, 3
	v_writelane_b32 v254, s27, 5
	v_writelane_b32 v254, s14, 7
	v_writelane_b32 v254, s15, 9
	v_writelane_b32 v254, s18, 11
	v_writelane_b32 v254, s20, 13
	s_mov_b32 s22, 0x42800000
	s_mov_b32 s19, 0
	v_writelane_b32 v254, s21, 14
	s_branch .LBB0_45

.LBB0_65:
	v_readlane_b32 s0, v253, 30
	s_add_u32 s4, s62, 0x10000
	s_mul_i32 s21, s14, s0
	s_addc_u32 s5, s63, 0
	v_readlane_b32 s33, v253, 38
	v_mov_b32_e32 v2, 0
	v_cmp_eq_u32_e64 s[2:3], 0, v166
	s_cmp_ge_i32 s21, s33
	s_cbranch_scc0 .Ldyn_go
	v_mov_b32_e32 v2, s33
	s_andn2_b64 s[2:3], s[2:3], s[2:3]
.Ldyn_go:
	s_and_saveexec_b64 s[0:1], s[2:3]
	v_readlane_b32 s39, v253, 36
	v_readlane_b32 s33, v253, 38
	s_cbranch_execz .LBB0_69
	s_mov_b64 s[8:9], exec
	v_mbcnt_lo_u32_b32 v2, s8, 0
	v_mbcnt_hi_u32_b32 v2, s9, v2
	v_cmp_eq_u32_e32 vcc, 0, v2
	s_and_saveexec_b64 s[6:7], vcc
	s_cbranch_execz .LBB0_68
	s_bcnt1_i32_b64 s8, s[8:9]
	v_mov_b32_e32 v3, 0
	v_mov_b32_e32 v4, s8
	global_atomic_add v3, v3, v4, s[4:5] sc0
